# indexer pass C2: stores use scalar base plus 32-bit lane offset instead of 64-bit per-lane addresses
# speedup vs baseline: 1.0068x; 1.0027x over previous
.LBB0_708:
	s_or_b64 exec, exec, s[0:1]
	v_add_u32_e32 v15, v16, v15
	v_sub_u32_sdwa v13, v15, v13 dst_sel:DWORD dst_unused:UNUSED_PAD src0_sel:WORD_0 src1_sel:DWORD
	v_sub_u32_sdwa v15, v15, v14 dst_sel:DWORD dst_unused:UNUSED_PAD src0_sel:WORD_1 src1_sel:DWORD
	v_add_u32_e32 v4, v13, v4
	v_add_u32_e32 v5, v15, v5
	v_lshl_or_b32 v14, v15, 16, v13
	v_lshl_or_b32 v15, v5, 16, v4
	v_add_u32_e32 v4, v4, v6
	v_add_u32_e32 v5, v5, v7
	v_lshl_or_b32 v16, v5, 16, v4
	v_add_u32_e32 v4, v4, v8
	v_add_u32_e32 v5, v5, v9
	v_lshl_or_b32 v17, v5, 16, v4
	s_and_b64 vcc, exec, s[16:17]
	ds_write_b128 v247, v[14:17] offset:3072
	s_waitcnt lgkmcnt(0)
	s_barrier
	s_cbranch_vccz .LBB0_358
	v_lshl_add_u64 v[4:5], s[94:95], 0, v[10:11]
	v_readlane_b32 s0, v255, 4
	ds_read2_b32 v[36:37], v12 offset0:64 offset1:96
	v_lshlrev_b64 v[4:5], 9, v[4:5]
	v_readlane_b32 s1, v255, 5
	v_lshlrev_b32_e32 v40, 4, v2
	v_mov_b32_e32 v41, v3
	v_lshl_add_u64 v[38:39], s[0:1], 0, v[4:5]
	s_mov_b64 s[38:39], s[0:1]
	v_mov_b32_e32 v54, v4
	v_readlane_b32 s0, v255, 19
	v_lshlrev_b32_e32 v4, 5, v10
	v_ashrrev_i32_e32 v5, 31, v4
	v_lshl_add_u32 v49, v10, 10, s0
	v_readlane_b32 s0, v255, 20
	v_readlane_b32 s1, v255, 21
	v_cmp_eq_u32_e64 s[22:23], 0, v2
	s_mov_b64 s[16:17], s[66:67]
	v_lshl_add_u64 v[42:43], s[0:1], 0, v[4:5]
	s_mov_b32 s36, s58
	s_mov_b64 s[40:41], 0x2000
	s_mov_b64 s[42:43], 0x8000
	s_waitcnt lgkmcnt(0)
	v_add_u32_e32 v52, -1, v36
	v_sub_u32_e32 v53, v36, v37
	s_branch .LBB0_712

.LBB0_718:
	v_lshl_add_u64 v[8:9], v[6:7], 1, s[12:13]
	global_load_dwordx4 v[4:7], v[8:9], off offset:16
	s_nop 0
	global_load_dwordx4 v[8:11], v[8:9], off
	s_and_saveexec_b64 s[24:25], vcc
	s_cbranch_execz .LBB0_845
	ds_read_u16 v2, v49 offset:36864
	v_add_u32_e32 v44, 0x11200, v49
	ds_read_b32 v44, v44
	s_waitcnt vmcnt(6)
	s_waitcnt lgkmcnt(1)
	v_lshrrev_b32_e32 v45, 8, v2
	v_and_b32_e32 v2, 0xff, v2
	v_cndmask_b32_e64 v45, v45, 0, s[22:23]
	v_cndmask_b32_e64 v2, v2, 0, s[22:23]
	s_waitcnt lgkmcnt(0)
	v_add_u32_sdwa v51, v45, v44 dst_sel:DWORD dst_unused:UNUSED_PAD src0_sel:DWORD src1_sel:WORD_1
	v_add_u32_sdwa v214, v2, v44 dst_sel:DWORD dst_unused:UNUSED_PAD src0_sel:DWORD src1_sel:WORD_0
	v_lshl_add_u64 v[44:45], v[40:41], 0, s[16:17]
	v_min_i32_e32 v2, v51, v37
	v_add_u32_e32 v2, v2, v214
	v_add_u32_e32 v51, v53, v51
	v_med3_i32 v214, v51, v52, v36
	v_cmp_gt_i32_sdwa s[0:1], v32, v214 src0_sel:WORD_0 src1_sel:DWORD
	v_cmp_eq_u32_sdwa s[30:31], v32, v36 src0_sel:WORD_0 src1_sel:DWORD
	v_lshl_add_u32 v46, v2, 1, v54
	s_and_saveexec_b64 s[34:35], s[0:1]
	global_store_short v46, v44, s[38:39]
	s_mov_b64 exec, s[34:35]
	v_addc_co_u32_e64 v2, vcc, 0, v2, s[0:1]
	v_addc_co_u32_e64 v51, vcc, 0, v51, s[30:31]
	v_lshl_add_u64 v[46:47], v[44:45], 0, 1
	v_med3_i32 v214, v51, v52, v36
	v_cmp_gt_i32_sdwa s[0:1], v32, v214 src0_sel:WORD_1 src1_sel:DWORD
	v_cmp_eq_u32_sdwa s[30:31], v32, v36 src0_sel:WORD_1 src1_sel:DWORD
	v_lshl_add_u32 v212, v2, 1, v54
	s_and_saveexec_b64 s[34:35], s[0:1]
	global_store_short v212, v46, s[38:39]
	s_mov_b64 exec, s[34:35]
	v_addc_co_u32_e64 v2, vcc, 0, v2, s[0:1]
	v_addc_co_u32_e64 v51, vcc, 0, v51, s[30:31]
	v_lshl_add_u64 v[46:47], v[44:45], 0, 2
	v_med3_i32 v214, v51, v52, v36
	v_cmp_gt_i32_sdwa s[0:1], v33, v214 src0_sel:WORD_0 src1_sel:DWORD
	v_cmp_eq_u32_sdwa s[30:31], v33, v36 src0_sel:WORD_0 src1_sel:DWORD
	v_lshl_add_u32 v212, v2, 1, v54
	s_and_saveexec_b64 s[34:35], s[0:1]
	global_store_short v212, v46, s[38:39]
	s_mov_b64 exec, s[34:35]
	v_addc_co_u32_e64 v2, vcc, 0, v2, s[0:1]
	v_addc_co_u32_e64 v51, vcc, 0, v51, s[30:31]
	v_lshl_add_u64 v[46:47], v[44:45], 0, 3
	v_med3_i32 v214, v51, v52, v36
	v_cmp_gt_i32_sdwa s[0:1], v33, v214 src0_sel:WORD_1 src1_sel:DWORD
	v_cmp_eq_u32_sdwa s[30:31], v33, v36 src0_sel:WORD_1 src1_sel:DWORD
	v_lshl_add_u32 v32, v2, 1, v54
	s_and_saveexec_b64 s[34:35], s[0:1]
	global_store_short v32, v46, s[38:39]
	s_mov_b64 exec, s[34:35]
	v_addc_co_u32_e64 v2, vcc, 0, v2, s[0:1]
	v_addc_co_u32_e64 v51, vcc, 0, v51, s[30:31]
	v_lshl_add_u64 v[32:33], v[44:45], 0, 4
	v_med3_i32 v214, v51, v52, v36
	v_cmp_gt_i32_sdwa s[0:1], v34, v214 src0_sel:WORD_0 src1_sel:DWORD
	v_cmp_eq_u32_sdwa s[30:31], v34, v36 src0_sel:WORD_0 src1_sel:DWORD
	v_lshl_add_u32 v46, v2, 1, v54
	s_and_saveexec_b64 s[34:35], s[0:1]
	global_store_short v46, v32, s[38:39]
	s_mov_b64 exec, s[34:35]
	v_addc_co_u32_e64 v2, vcc, 0, v2, s[0:1]
	v_addc_co_u32_e64 v51, vcc, 0, v51, s[30:31]
	v_lshl_add_u64 v[32:33], v[44:45], 0, 5
	v_med3_i32 v214, v51, v52, v36
	v_cmp_gt_i32_sdwa s[0:1], v34, v214 src0_sel:WORD_1 src1_sel:DWORD
	v_cmp_eq_u32_sdwa s[30:31], v34, v36 src0_sel:WORD_1 src1_sel:DWORD
	v_lshl_add_u32 v46, v2, 1, v54
	s_and_saveexec_b64 s[34:35], s[0:1]
	global_store_short v46, v32, s[38:39]
	s_mov_b64 exec, s[34:35]
	v_addc_co_u32_e64 v2, vcc, 0, v2, s[0:1]
	v_addc_co_u32_e64 v51, vcc, 0, v51, s[30:31]
	v_lshl_add_u64 v[32:33], v[44:45], 0, 6
	v_med3_i32 v214, v51, v52, v36
	v_cmp_gt_i32_sdwa s[0:1], v35, v214 src0_sel:WORD_0 src1_sel:DWORD
	v_cmp_eq_u32_sdwa s[30:31], v35, v36 src0_sel:WORD_0 src1_sel:DWORD
	v_lshl_add_u32 v46, v2, 1, v54
	s_and_saveexec_b64 s[34:35], s[0:1]
	global_store_short v46, v32, s[38:39]
	s_mov_b64 exec, s[34:35]
	v_addc_co_u32_e64 v2, vcc, 0, v2, s[0:1]
	v_addc_co_u32_e64 v51, vcc, 0, v51, s[30:31]
	v_lshl_add_u64 v[32:33], v[44:45], 0, 7
	v_med3_i32 v214, v51, v52, v36
	v_cmp_gt_i32_sdwa s[0:1], v35, v214 src0_sel:WORD_1 src1_sel:DWORD
	v_cmp_eq_u32_sdwa s[30:31], v35, v36 src0_sel:WORD_1 src1_sel:DWORD
	v_lshl_add_u32 v34, v2, 1, v54
	s_and_saveexec_b64 s[34:35], s[0:1]
	global_store_short v34, v32, s[38:39]
	s_mov_b64 exec, s[34:35]
	v_addc_co_u32_e64 v2, vcc, 0, v2, s[0:1]
	v_addc_co_u32_e64 v51, vcc, 0, v51, s[30:31]
	v_lshl_add_u64 v[32:33], v[44:45], 0, 8
	v_med3_i32 v214, v51, v52, v36
	v_cmp_gt_i32_sdwa s[0:1], v28, v214 src0_sel:WORD_0 src1_sel:DWORD
	v_cmp_eq_u32_sdwa s[30:31], v28, v36 src0_sel:WORD_0 src1_sel:DWORD
	v_lshl_add_u32 v34, v2, 1, v54
	s_and_saveexec_b64 s[34:35], s[0:1]
	global_store_short v34, v32, s[38:39]
	s_mov_b64 exec, s[34:35]
	v_addc_co_u32_e64 v2, vcc, 0, v2, s[0:1]
	v_addc_co_u32_e64 v51, vcc, 0, v51, s[30:31]
	v_lshl_add_u64 v[32:33], v[44:45], 0, 9
	v_med3_i32 v214, v51, v52, v36
	v_cmp_gt_i32_sdwa s[0:1], v28, v214 src0_sel:WORD_1 src1_sel:DWORD
	v_cmp_eq_u32_sdwa s[30:31], v28, v36 src0_sel:WORD_1 src1_sel:DWORD
	v_lshl_add_u32 v34, v2, 1, v54
	s_and_saveexec_b64 s[34:35], s[0:1]
	global_store_short v34, v32, s[38:39]
	s_mov_b64 exec, s[34:35]
	v_addc_co_u32_e64 v2, vcc, 0, v2, s[0:1]
	v_addc_co_u32_e64 v51, vcc, 0, v51, s[30:31]
	v_lshl_add_u64 v[32:33], v[44:45], 0, 10
	v_med3_i32 v214, v51, v52, v36
	v_cmp_gt_i32_sdwa s[0:1], v29, v214 src0_sel:WORD_0 src1_sel:DWORD
	v_cmp_eq_u32_sdwa s[30:31], v29, v36 src0_sel:WORD_0 src1_sel:DWORD
	v_lshl_add_u32 v34, v2, 1, v54
	s_and_saveexec_b64 s[34:35], s[0:1]
	global_store_short v34, v32, s[38:39]
	s_mov_b64 exec, s[34:35]
	v_addc_co_u32_e64 v2, vcc, 0, v2, s[0:1]
	v_addc_co_u32_e64 v51, vcc, 0, v51, s[30:31]
	v_lshl_add_u64 v[32:33], v[44:45], 0, 11
	v_med3_i32 v214, v51, v52, v36
	v_cmp_gt_i32_sdwa s[0:1], v29, v214 src0_sel:WORD_1 src1_sel:DWORD
	v_cmp_eq_u32_sdwa s[30:31], v29, v36 src0_sel:WORD_1 src1_sel:DWORD
	v_lshl_add_u32 v28, v2, 1, v54
	s_and_saveexec_b64 s[34:35], s[0:1]
	global_store_short v28, v32, s[38:39]
	s_mov_b64 exec, s[34:35]
	v_addc_co_u32_e64 v2, vcc, 0, v2, s[0:1]
	v_addc_co_u32_e64 v51, vcc, 0, v51, s[30:31]
	v_lshl_add_u64 v[28:29], v[44:45], 0, 12
	v_med3_i32 v214, v51, v52, v36
	v_cmp_gt_i32_sdwa s[0:1], v30, v214 src0_sel:WORD_0 src1_sel:DWORD
	v_cmp_eq_u32_sdwa s[30:31], v30, v36 src0_sel:WORD_0 src1_sel:DWORD
	v_lshl_add_u32 v32, v2, 1, v54
	s_and_saveexec_b64 s[34:35], s[0:1]
	global_store_short v32, v28, s[38:39]
	s_mov_b64 exec, s[34:35]
	v_addc_co_u32_e64 v2, vcc, 0, v2, s[0:1]
	v_addc_co_u32_e64 v51, vcc, 0, v51, s[30:31]
	v_lshl_add_u64 v[28:29], v[44:45], 0, 13
	v_med3_i32 v214, v51, v52, v36
	v_cmp_gt_i32_sdwa s[0:1], v30, v214 src0_sel:WORD_1 src1_sel:DWORD
	v_cmp_eq_u32_sdwa s[30:31], v30, v36 src0_sel:WORD_1 src1_sel:DWORD
	v_lshl_add_u32 v32, v2, 1, v54
	s_and_saveexec_b64 s[34:35], s[0:1]
	global_store_short v32, v28, s[38:39]
	s_mov_b64 exec, s[34:35]
	v_addc_co_u32_e64 v2, vcc, 0, v2, s[0:1]
	v_addc_co_u32_e64 v51, vcc, 0, v51, s[30:31]
	v_lshl_add_u64 v[28:29], v[44:45], 0, 14
	v_med3_i32 v214, v51, v52, v36
	v_cmp_gt_i32_sdwa s[0:1], v31, v214 src0_sel:WORD_0 src1_sel:DWORD
	v_cmp_eq_u32_sdwa s[30:31], v31, v36 src0_sel:WORD_0 src1_sel:DWORD
	v_lshl_add_u32 v32, v2, 1, v54
	s_and_saveexec_b64 s[34:35], s[0:1]
	global_store_short v32, v28, s[38:39]
	s_mov_b64 exec, s[34:35]
	v_addc_co_u32_e64 v2, vcc, 0, v2, s[0:1]
	v_addc_co_u32_e64 v51, vcc, 0, v51, s[30:31]
	v_med3_i32 v214, v51, v52, v36
	v_cmp_gt_i32_sdwa s[30:31], v31, v214 src0_sel:WORD_1 src1_sel:DWORD
	v_lshl_add_u32 v28, v2, 1, v54
	v_or_b32_e32 v214, 15, v44
	s_and_saveexec_b64 s[34:35], s[30:31]
	global_store_short v28, v214, s[38:39]
	s_mov_b64 exec, s[34:35]
.LBB0_843:
.LBB0_844:
.LBB0_845:
	s_or_b64 exec, exec, s[24:25]
	s_andn2_b64 vcc, exec, s[18:19]
	s_cbranch_vccnz .LBB0_975
	ds_read_u16 v2, v50 offset:36896
	s_waitcnt lgkmcnt(0)
	v_cmp_ne_u16_e32 vcc, 0, v2
	s_and_saveexec_b64 s[18:19], vcc
	s_cbranch_execz .LBB0_973
	ds_read_u16 v2, v49 offset:36896
	s_waitcnt vmcnt(7)
	v_add_u32_e32 v28, 0x11220, v49
	ds_read_b32 v28, v28
	v_lshl_add_u64 v[30:31], v[40:41], 0, s[16:17]
	s_waitcnt vmcnt(4)
	s_waitcnt lgkmcnt(1)
	v_lshrrev_b32_e32 v29, 8, v2
	v_and_b32_e32 v2, 0xff, v2
	v_cndmask_b32_e64 v29, v29, 0, s[22:23]
	v_cndmask_b32_e64 v2, v2, 0, s[22:23]
	s_waitcnt lgkmcnt(0)
	v_add_u32_sdwa v34, v29, v28 dst_sel:DWORD dst_unused:UNUSED_PAD src0_sel:DWORD src1_sel:WORD_1
	v_add_u32_sdwa v35, v2, v28 dst_sel:DWORD dst_unused:UNUSED_PAD src0_sel:DWORD src1_sel:WORD_0
	v_lshl_add_u64 v[28:29], v[30:31], 0, s[84:85]
	v_min_i32_e32 v2, v34, v37
	v_add_u32_e32 v2, v2, v35
	v_add_u32_e32 v34, v53, v34
	v_med3_i32 v35, v34, v52, v36
	v_cmp_gt_i32_sdwa s[0:1], v24, v35 src0_sel:WORD_0 src1_sel:DWORD
	v_cmp_eq_u32_sdwa s[24:25], v24, v36 src0_sel:WORD_0 src1_sel:DWORD
	v_lshl_add_u32 v32, v2, 1, v54
	s_and_saveexec_b64 s[30:31], s[0:1]
	global_store_short v32, v28, s[38:39]
	s_mov_b64 exec, s[30:31]
	v_addc_co_u32_e64 v2, vcc, 0, v2, s[0:1]
	v_addc_co_u32_e64 v34, vcc, 0, v34, s[24:25]
	v_add_u32_e32 v32, 0x101, v30
	v_med3_i32 v35, v34, v52, v36
	v_cmp_gt_i32_sdwa s[0:1], v24, v35 src0_sel:WORD_1 src1_sel:DWORD
	v_cmp_eq_u32_sdwa s[24:25], v24, v36 src0_sel:WORD_1 src1_sel:DWORD
	v_lshl_add_u32 v44, v2, 1, v54
	s_and_saveexec_b64 s[30:31], s[0:1]
	global_store_short v44, v32, s[38:39]
	s_mov_b64 exec, s[30:31]
	v_addc_co_u32_e64 v2, vcc, 0, v2, s[0:1]
	v_addc_co_u32_e64 v34, vcc, 0, v34, s[24:25]
	v_add_u32_e32 v32, 0x102, v30
	v_med3_i32 v35, v34, v52, v36
	v_cmp_gt_i32_sdwa s[0:1], v25, v35 src0_sel:WORD_0 src1_sel:DWORD
	v_cmp_eq_u32_sdwa s[24:25], v25, v36 src0_sel:WORD_0 src1_sel:DWORD
	v_lshl_add_u32 v44, v2, 1, v54
	s_and_saveexec_b64 s[30:31], s[0:1]
	global_store_short v44, v32, s[38:39]
	s_mov_b64 exec, s[30:31]
	v_addc_co_u32_e64 v2, vcc, 0, v2, s[0:1]
	v_addc_co_u32_e64 v34, vcc, 0, v34, s[24:25]
	v_add_u32_e32 v32, 0x103, v30
	v_med3_i32 v35, v34, v52, v36
	v_cmp_gt_i32_sdwa s[0:1], v25, v35 src0_sel:WORD_1 src1_sel:DWORD
	v_cmp_eq_u32_sdwa s[24:25], v25, v36 src0_sel:WORD_1 src1_sel:DWORD
	v_lshl_add_u32 v24, v2, 1, v54
	s_and_saveexec_b64 s[30:31], s[0:1]
	global_store_short v24, v32, s[38:39]
	s_mov_b64 exec, s[30:31]
	v_addc_co_u32_e64 v2, vcc, 0, v2, s[0:1]
	v_addc_co_u32_e64 v34, vcc, 0, v34, s[24:25]
	v_add_u32_e32 v24, 0x104, v30
	v_med3_i32 v35, v34, v52, v36
	v_cmp_gt_i32_sdwa s[0:1], v26, v35 src0_sel:WORD_0 src1_sel:DWORD
	v_cmp_eq_u32_sdwa s[24:25], v26, v36 src0_sel:WORD_0 src1_sel:DWORD
	v_lshl_add_u32 v32, v2, 1, v54
	s_and_saveexec_b64 s[30:31], s[0:1]
	global_store_short v32, v24, s[38:39]
	s_mov_b64 exec, s[30:31]
	v_addc_co_u32_e64 v2, vcc, 0, v2, s[0:1]
	v_addc_co_u32_e64 v34, vcc, 0, v34, s[24:25]
	v_add_u32_e32 v24, 0x105, v30
	v_med3_i32 v35, v34, v52, v36
	v_cmp_gt_i32_sdwa s[0:1], v26, v35 src0_sel:WORD_1 src1_sel:DWORD
	v_cmp_eq_u32_sdwa s[24:25], v26, v36 src0_sel:WORD_1 src1_sel:DWORD
	v_lshl_add_u32 v32, v2, 1, v54
	s_and_saveexec_b64 s[30:31], s[0:1]
	global_store_short v32, v24, s[38:39]
	s_mov_b64 exec, s[30:31]
	v_addc_co_u32_e64 v2, vcc, 0, v2, s[0:1]
	v_addc_co_u32_e64 v34, vcc, 0, v34, s[24:25]
	v_add_u32_e32 v24, 0x106, v30
	v_med3_i32 v35, v34, v52, v36
	v_cmp_gt_i32_sdwa s[0:1], v27, v35 src0_sel:WORD_0 src1_sel:DWORD
	v_cmp_eq_u32_sdwa s[24:25], v27, v36 src0_sel:WORD_0 src1_sel:DWORD
	v_lshl_add_u32 v32, v2, 1, v54
	s_and_saveexec_b64 s[30:31], s[0:1]
	global_store_short v32, v24, s[38:39]
	s_mov_b64 exec, s[30:31]
	v_addc_co_u32_e64 v2, vcc, 0, v2, s[0:1]
	v_addc_co_u32_e64 v34, vcc, 0, v34, s[24:25]
	v_add_u32_e32 v24, 0x107, v30
	v_med3_i32 v35, v34, v52, v36
	v_cmp_gt_i32_sdwa s[0:1], v27, v35 src0_sel:WORD_1 src1_sel:DWORD
	v_cmp_eq_u32_sdwa s[24:25], v27, v36 src0_sel:WORD_1 src1_sel:DWORD
	v_lshl_add_u32 v26, v2, 1, v54
	s_and_saveexec_b64 s[30:31], s[0:1]
	global_store_short v26, v24, s[38:39]
	s_mov_b64 exec, s[30:31]
	v_addc_co_u32_e64 v2, vcc, 0, v2, s[0:1]
	v_addc_co_u32_e64 v34, vcc, 0, v34, s[24:25]
	v_add_u32_e32 v24, 0x108, v30
	v_med3_i32 v35, v34, v52, v36
	v_cmp_gt_i32_sdwa s[0:1], v20, v35 src0_sel:WORD_0 src1_sel:DWORD
	v_cmp_eq_u32_sdwa s[24:25], v20, v36 src0_sel:WORD_0 src1_sel:DWORD
	v_lshl_add_u32 v26, v2, 1, v54
	s_and_saveexec_b64 s[30:31], s[0:1]
	global_store_short v26, v24, s[38:39]
	s_mov_b64 exec, s[30:31]
	v_addc_co_u32_e64 v2, vcc, 0, v2, s[0:1]
	v_addc_co_u32_e64 v34, vcc, 0, v34, s[24:25]
	v_add_u32_e32 v24, 0x109, v30
	v_med3_i32 v35, v34, v52, v36
	v_cmp_gt_i32_sdwa s[0:1], v20, v35 src0_sel:WORD_1 src1_sel:DWORD
	v_cmp_eq_u32_sdwa s[24:25], v20, v36 src0_sel:WORD_1 src1_sel:DWORD
	v_lshl_add_u32 v26, v2, 1, v54
	s_and_saveexec_b64 s[30:31], s[0:1]
	global_store_short v26, v24, s[38:39]
	s_mov_b64 exec, s[30:31]
	v_addc_co_u32_e64 v2, vcc, 0, v2, s[0:1]
	v_addc_co_u32_e64 v34, vcc, 0, v34, s[24:25]
	v_add_u32_e32 v24, 0x10a, v30
	v_med3_i32 v35, v34, v52, v36
	v_cmp_gt_i32_sdwa s[0:1], v21, v35 src0_sel:WORD_0 src1_sel:DWORD
	v_cmp_eq_u32_sdwa s[24:25], v21, v36 src0_sel:WORD_0 src1_sel:DWORD
	v_lshl_add_u32 v26, v2, 1, v54
	s_and_saveexec_b64 s[30:31], s[0:1]
	global_store_short v26, v24, s[38:39]
	s_mov_b64 exec, s[30:31]
	v_addc_co_u32_e64 v2, vcc, 0, v2, s[0:1]
	v_addc_co_u32_e64 v34, vcc, 0, v34, s[24:25]
	v_add_u32_e32 v24, 0x10b, v30
	v_med3_i32 v35, v34, v52, v36
	v_cmp_gt_i32_sdwa s[0:1], v21, v35 src0_sel:WORD_1 src1_sel:DWORD
	v_cmp_eq_u32_sdwa s[24:25], v21, v36 src0_sel:WORD_1 src1_sel:DWORD
	v_lshl_add_u32 v20, v2, 1, v54
	s_and_saveexec_b64 s[30:31], s[0:1]
	global_store_short v20, v24, s[38:39]
	s_mov_b64 exec, s[30:31]
	v_addc_co_u32_e64 v2, vcc, 0, v2, s[0:1]
	v_addc_co_u32_e64 v34, vcc, 0, v34, s[24:25]
	v_add_u32_e32 v20, 0x10c, v30
	v_med3_i32 v35, v34, v52, v36
	v_cmp_gt_i32_sdwa s[0:1], v22, v35 src0_sel:WORD_0 src1_sel:DWORD
	v_cmp_eq_u32_sdwa s[24:25], v22, v36 src0_sel:WORD_0 src1_sel:DWORD
	v_lshl_add_u32 v24, v2, 1, v54
	s_and_saveexec_b64 s[30:31], s[0:1]
	global_store_short v24, v20, s[38:39]
	s_mov_b64 exec, s[30:31]
	v_addc_co_u32_e64 v2, vcc, 0, v2, s[0:1]
	v_addc_co_u32_e64 v34, vcc, 0, v34, s[24:25]
	v_add_u32_e32 v20, 0x10d, v30
	v_med3_i32 v35, v34, v52, v36
	v_cmp_gt_i32_sdwa s[0:1], v22, v35 src0_sel:WORD_1 src1_sel:DWORD
	v_cmp_eq_u32_sdwa s[24:25], v22, v36 src0_sel:WORD_1 src1_sel:DWORD
	v_lshl_add_u32 v24, v2, 1, v54
	s_and_saveexec_b64 s[30:31], s[0:1]
	global_store_short v24, v20, s[38:39]
	s_mov_b64 exec, s[30:31]
	v_addc_co_u32_e64 v2, vcc, 0, v2, s[0:1]
	v_addc_co_u32_e64 v34, vcc, 0, v34, s[24:25]
	v_add_u32_e32 v20, 0x10e, v30
	v_med3_i32 v35, v34, v52, v36
	v_cmp_gt_i32_sdwa s[0:1], v23, v35 src0_sel:WORD_0 src1_sel:DWORD
	v_cmp_eq_u32_sdwa s[24:25], v23, v36 src0_sel:WORD_0 src1_sel:DWORD
	v_lshl_add_u32 v24, v2, 1, v54
	s_and_saveexec_b64 s[30:31], s[0:1]
	global_store_short v24, v20, s[38:39]
	s_mov_b64 exec, s[30:31]
	v_addc_co_u32_e64 v2, vcc, 0, v2, s[0:1]
	v_addc_co_u32_e64 v34, vcc, 0, v34, s[24:25]
	v_med3_i32 v35, v34, v52, v36
	v_cmp_gt_i32_sdwa s[24:25], v23, v35 src0_sel:WORD_1 src1_sel:DWORD
	v_lshl_add_u32 v20, v2, 1, v54
	v_or_b32_e32 v35, 15, v28
	s_and_saveexec_b64 s[30:31], s[24:25]
	global_store_short v20, v35, s[38:39]
	s_mov_b64 exec, s[30:31]

.LBB0_976:
	ds_read_u16 v2, v50 offset:36928
	s_waitcnt lgkmcnt(0)
	v_cmp_ne_u16_e32 vcc, 0, v2
	s_and_saveexec_b64 s[18:19], vcc
	s_cbranch_execz .LBB0_1103
	ds_read_u16 v2, v49 offset:36928
	s_waitcnt vmcnt(5)
	v_add_u32_e32 v20, 0x11240, v49
	ds_read_b32 v20, v20
	v_lshl_add_u64 v[22:23], v[40:41], 0, s[16:17]
	s_mov_b64 s[0:1], 0x200
	s_waitcnt lgkmcnt(1)
	v_lshrrev_b32_e32 v21, 8, v2
	v_and_b32_e32 v2, 0xff, v2
	v_cndmask_b32_e64 v21, v21, 0, s[22:23]
	v_cndmask_b32_e64 v2, v2, 0, s[22:23]
	s_waitcnt vmcnt(4) lgkmcnt(0)
	v_add_u32_sdwa v26, v21, v20 dst_sel:DWORD dst_unused:UNUSED_PAD src0_sel:DWORD src1_sel:WORD_1
	v_add_u32_sdwa v27, v2, v20 dst_sel:DWORD dst_unused:UNUSED_PAD src0_sel:DWORD src1_sel:WORD_0
	v_lshl_add_u64 v[20:21], v[22:23], 0, s[0:1]
	s_waitcnt vmcnt(2)
	v_min_i32_e32 v2, v26, v37
	v_add_u32_e32 v2, v2, v27
	v_add_u32_e32 v26, v53, v26
	v_med3_i32 v27, v26, v52, v36
	v_cmp_gt_i32_sdwa s[0:1], v16, v27 src0_sel:WORD_0 src1_sel:DWORD
	v_cmp_eq_u32_sdwa s[24:25], v16, v36 src0_sel:WORD_0 src1_sel:DWORD
	v_lshl_add_u32 v24, v2, 1, v54
	s_and_saveexec_b64 s[28:29], s[0:1]
	global_store_short v24, v20, s[38:39]
	s_mov_b64 exec, s[28:29]
	v_addc_co_u32_e64 v2, vcc, 0, v2, s[0:1]
	v_addc_co_u32_e64 v26, vcc, 0, v26, s[24:25]
	v_add_u32_e32 v24, 0x201, v22
	v_med3_i32 v27, v26, v52, v36
	v_cmp_gt_i32_sdwa s[0:1], v16, v27 src0_sel:WORD_1 src1_sel:DWORD
	v_cmp_eq_u32_sdwa s[24:25], v16, v36 src0_sel:WORD_1 src1_sel:DWORD
	v_lshl_add_u32 v28, v2, 1, v54
	s_and_saveexec_b64 s[28:29], s[0:1]
	global_store_short v28, v24, s[38:39]
	s_mov_b64 exec, s[28:29]
	v_addc_co_u32_e64 v2, vcc, 0, v2, s[0:1]
	v_addc_co_u32_e64 v26, vcc, 0, v26, s[24:25]
	v_add_u32_e32 v24, 0x202, v22
	v_med3_i32 v27, v26, v52, v36
	v_cmp_gt_i32_sdwa s[0:1], v17, v27 src0_sel:WORD_0 src1_sel:DWORD
	v_cmp_eq_u32_sdwa s[24:25], v17, v36 src0_sel:WORD_0 src1_sel:DWORD
	v_lshl_add_u32 v28, v2, 1, v54
	s_and_saveexec_b64 s[28:29], s[0:1]
	global_store_short v28, v24, s[38:39]
	s_mov_b64 exec, s[28:29]
	v_addc_co_u32_e64 v2, vcc, 0, v2, s[0:1]
	v_addc_co_u32_e64 v26, vcc, 0, v26, s[24:25]
	v_add_u32_e32 v24, 0x203, v22
	v_med3_i32 v27, v26, v52, v36
	v_cmp_gt_i32_sdwa s[0:1], v17, v27 src0_sel:WORD_1 src1_sel:DWORD
	v_cmp_eq_u32_sdwa s[24:25], v17, v36 src0_sel:WORD_1 src1_sel:DWORD
	v_lshl_add_u32 v16, v2, 1, v54
	s_and_saveexec_b64 s[28:29], s[0:1]
	global_store_short v16, v24, s[38:39]
	s_mov_b64 exec, s[28:29]
	v_addc_co_u32_e64 v2, vcc, 0, v2, s[0:1]
	v_addc_co_u32_e64 v26, vcc, 0, v26, s[24:25]
	v_add_u32_e32 v16, 0x204, v22
	v_med3_i32 v27, v26, v52, v36
	v_cmp_gt_i32_sdwa s[0:1], v18, v27 src0_sel:WORD_0 src1_sel:DWORD
	v_cmp_eq_u32_sdwa s[24:25], v18, v36 src0_sel:WORD_0 src1_sel:DWORD
	v_lshl_add_u32 v24, v2, 1, v54
	s_and_saveexec_b64 s[28:29], s[0:1]
	global_store_short v24, v16, s[38:39]
	s_mov_b64 exec, s[28:29]
	v_addc_co_u32_e64 v2, vcc, 0, v2, s[0:1]
	v_addc_co_u32_e64 v26, vcc, 0, v26, s[24:25]
	v_add_u32_e32 v16, 0x205, v22
	v_med3_i32 v27, v26, v52, v36
	v_cmp_gt_i32_sdwa s[0:1], v18, v27 src0_sel:WORD_1 src1_sel:DWORD
	v_cmp_eq_u32_sdwa s[24:25], v18, v36 src0_sel:WORD_1 src1_sel:DWORD
	v_lshl_add_u32 v24, v2, 1, v54
	s_and_saveexec_b64 s[28:29], s[0:1]
	global_store_short v24, v16, s[38:39]
	s_mov_b64 exec, s[28:29]
	v_addc_co_u32_e64 v2, vcc, 0, v2, s[0:1]
	v_addc_co_u32_e64 v26, vcc, 0, v26, s[24:25]
	v_add_u32_e32 v16, 0x206, v22
	v_med3_i32 v27, v26, v52, v36
	v_cmp_gt_i32_sdwa s[0:1], v19, v27 src0_sel:WORD_0 src1_sel:DWORD
	v_cmp_eq_u32_sdwa s[24:25], v19, v36 src0_sel:WORD_0 src1_sel:DWORD
	v_lshl_add_u32 v24, v2, 1, v54
	s_and_saveexec_b64 s[28:29], s[0:1]
	global_store_short v24, v16, s[38:39]
	s_mov_b64 exec, s[28:29]
	v_addc_co_u32_e64 v2, vcc, 0, v2, s[0:1]
	v_addc_co_u32_e64 v26, vcc, 0, v26, s[24:25]
	v_add_u32_e32 v16, 0x207, v22
	v_med3_i32 v27, v26, v52, v36
	v_cmp_gt_i32_sdwa s[0:1], v19, v27 src0_sel:WORD_1 src1_sel:DWORD
	v_cmp_eq_u32_sdwa s[24:25], v19, v36 src0_sel:WORD_1 src1_sel:DWORD
	v_lshl_add_u32 v18, v2, 1, v54
	s_and_saveexec_b64 s[28:29], s[0:1]
	global_store_short v18, v16, s[38:39]
	s_mov_b64 exec, s[28:29]
	v_addc_co_u32_e64 v2, vcc, 0, v2, s[0:1]
	v_addc_co_u32_e64 v26, vcc, 0, v26, s[24:25]
	v_add_u32_e32 v16, 0x208, v22
	v_med3_i32 v27, v26, v52, v36
	v_cmp_gt_i32_sdwa s[0:1], v12, v27 src0_sel:WORD_0 src1_sel:DWORD
	v_cmp_eq_u32_sdwa s[24:25], v12, v36 src0_sel:WORD_0 src1_sel:DWORD
	v_lshl_add_u32 v18, v2, 1, v54
	s_and_saveexec_b64 s[28:29], s[0:1]
	global_store_short v18, v16, s[38:39]
	s_mov_b64 exec, s[28:29]
	v_addc_co_u32_e64 v2, vcc, 0, v2, s[0:1]
	v_addc_co_u32_e64 v26, vcc, 0, v26, s[24:25]
	v_add_u32_e32 v16, 0x209, v22
	v_med3_i32 v27, v26, v52, v36
	v_cmp_gt_i32_sdwa s[0:1], v12, v27 src0_sel:WORD_1 src1_sel:DWORD
	v_cmp_eq_u32_sdwa s[24:25], v12, v36 src0_sel:WORD_1 src1_sel:DWORD
	v_lshl_add_u32 v18, v2, 1, v54
	s_and_saveexec_b64 s[28:29], s[0:1]
	global_store_short v18, v16, s[38:39]
	s_mov_b64 exec, s[28:29]
	v_addc_co_u32_e64 v2, vcc, 0, v2, s[0:1]
	v_addc_co_u32_e64 v26, vcc, 0, v26, s[24:25]
	v_add_u32_e32 v16, 0x20a, v22
	v_med3_i32 v27, v26, v52, v36
	v_cmp_gt_i32_sdwa s[0:1], v13, v27 src0_sel:WORD_0 src1_sel:DWORD
	v_cmp_eq_u32_sdwa s[24:25], v13, v36 src0_sel:WORD_0 src1_sel:DWORD
	v_lshl_add_u32 v18, v2, 1, v54
	s_and_saveexec_b64 s[28:29], s[0:1]
	global_store_short v18, v16, s[38:39]
	s_mov_b64 exec, s[28:29]
	v_addc_co_u32_e64 v2, vcc, 0, v2, s[0:1]
	v_addc_co_u32_e64 v26, vcc, 0, v26, s[24:25]
	v_add_u32_e32 v16, 0x20b, v22
	v_med3_i32 v27, v26, v52, v36
	v_cmp_gt_i32_sdwa s[0:1], v13, v27 src0_sel:WORD_1 src1_sel:DWORD
	v_cmp_eq_u32_sdwa s[24:25], v13, v36 src0_sel:WORD_1 src1_sel:DWORD
	v_lshl_add_u32 v12, v2, 1, v54
	s_and_saveexec_b64 s[28:29], s[0:1]
	global_store_short v12, v16, s[38:39]
	s_mov_b64 exec, s[28:29]
	v_addc_co_u32_e64 v2, vcc, 0, v2, s[0:1]
	v_addc_co_u32_e64 v26, vcc, 0, v26, s[24:25]
	v_add_u32_e32 v12, 0x20c, v22
	v_med3_i32 v27, v26, v52, v36
	v_cmp_gt_i32_sdwa s[0:1], v14, v27 src0_sel:WORD_0 src1_sel:DWORD
	v_cmp_eq_u32_sdwa s[24:25], v14, v36 src0_sel:WORD_0 src1_sel:DWORD
	v_lshl_add_u32 v16, v2, 1, v54
	s_and_saveexec_b64 s[28:29], s[0:1]
	global_store_short v16, v12, s[38:39]
	s_mov_b64 exec, s[28:29]
	v_addc_co_u32_e64 v2, vcc, 0, v2, s[0:1]
	v_addc_co_u32_e64 v26, vcc, 0, v26, s[24:25]
	v_add_u32_e32 v12, 0x20d, v22
	v_med3_i32 v27, v26, v52, v36
	v_cmp_gt_i32_sdwa s[0:1], v14, v27 src0_sel:WORD_1 src1_sel:DWORD
	v_cmp_eq_u32_sdwa s[24:25], v14, v36 src0_sel:WORD_1 src1_sel:DWORD
	v_lshl_add_u32 v16, v2, 1, v54
	s_and_saveexec_b64 s[28:29], s[0:1]
	global_store_short v16, v12, s[38:39]
	s_mov_b64 exec, s[28:29]
	v_addc_co_u32_e64 v2, vcc, 0, v2, s[0:1]
	v_addc_co_u32_e64 v26, vcc, 0, v26, s[24:25]
	v_add_u32_e32 v12, 0x20e, v22
	v_med3_i32 v27, v26, v52, v36
	v_cmp_gt_i32_sdwa s[0:1], v15, v27 src0_sel:WORD_0 src1_sel:DWORD
	v_cmp_eq_u32_sdwa s[24:25], v15, v36 src0_sel:WORD_0 src1_sel:DWORD
	v_lshl_add_u32 v16, v2, 1, v54
	s_and_saveexec_b64 s[28:29], s[0:1]
	global_store_short v16, v12, s[38:39]
	s_mov_b64 exec, s[28:29]
	v_addc_co_u32_e64 v2, vcc, 0, v2, s[0:1]
	v_addc_co_u32_e64 v26, vcc, 0, v26, s[24:25]
	v_med3_i32 v27, v26, v52, v36
	v_cmp_gt_i32_sdwa s[24:25], v15, v27 src0_sel:WORD_1 src1_sel:DWORD
	v_lshl_add_u32 v12, v2, 1, v54
	v_or_b32_e32 v27, 15, v20
	s_and_saveexec_b64 s[28:29], s[24:25]
	global_store_short v12, v27, s[38:39]
	s_mov_b64 exec, s[28:29]

.LBB0_1104:
	ds_read_u16 v2, v50 offset:36960
	s_waitcnt lgkmcnt(0)
	v_cmp_ne_u16_e32 vcc, 0, v2
	s_and_saveexec_b64 s[18:19], vcc
	s_cbranch_execz .LBB0_710
	ds_read_u16 v2, v49 offset:36960
	s_waitcnt vmcnt(3)
	v_add_u32_e32 v12, 0x11260, v49
	ds_read_b32 v12, v12
	v_lshl_add_u64 v[14:15], v[40:41], 0, s[16:17]
	s_mov_b64 s[0:1], 0x300
	s_waitcnt lgkmcnt(1)
	v_lshrrev_b32_e32 v13, 8, v2
	v_and_b32_e32 v2, 0xff, v2
	v_cndmask_b32_e64 v13, v13, 0, s[22:23]
	v_cndmask_b32_e64 v2, v2, 0, s[22:23]
	s_waitcnt vmcnt(2) lgkmcnt(0)
	v_add_u32_sdwa v18, v13, v12 dst_sel:DWORD dst_unused:UNUSED_PAD src0_sel:DWORD src1_sel:WORD_1
	v_add_u32_sdwa v19, v2, v12 dst_sel:DWORD dst_unused:UNUSED_PAD src0_sel:DWORD src1_sel:WORD_0
	v_lshl_add_u64 v[12:13], v[14:15], 0, s[0:1]
	s_waitcnt vmcnt(0)
	v_min_i32_e32 v2, v18, v37
	v_add_u32_e32 v2, v2, v19
	v_add_u32_e32 v18, v53, v18
	v_med3_i32 v19, v18, v52, v36
	v_cmp_gt_i32_sdwa s[0:1], v8, v19 src0_sel:WORD_0 src1_sel:DWORD
	v_cmp_eq_u32_sdwa s[24:25], v8, v36 src0_sel:WORD_0 src1_sel:DWORD
	v_lshl_add_u32 v16, v2, 1, v54
	s_and_saveexec_b64 s[26:27], s[0:1]
	global_store_short v16, v12, s[38:39]
	s_mov_b64 exec, s[26:27]
	v_addc_co_u32_e64 v2, vcc, 0, v2, s[0:1]
	v_addc_co_u32_e64 v18, vcc, 0, v18, s[24:25]
	v_add_u32_e32 v16, 0x301, v14
	v_med3_i32 v19, v18, v52, v36
	v_cmp_gt_i32_sdwa s[0:1], v8, v19 src0_sel:WORD_1 src1_sel:DWORD
	v_cmp_eq_u32_sdwa s[24:25], v8, v36 src0_sel:WORD_1 src1_sel:DWORD
	v_lshl_add_u32 v20, v2, 1, v54
	s_and_saveexec_b64 s[26:27], s[0:1]
	global_store_short v20, v16, s[38:39]
	s_mov_b64 exec, s[26:27]
	v_addc_co_u32_e64 v2, vcc, 0, v2, s[0:1]
	v_addc_co_u32_e64 v18, vcc, 0, v18, s[24:25]
	v_add_u32_e32 v16, 0x302, v14
	v_med3_i32 v19, v18, v52, v36
	v_cmp_gt_i32_sdwa s[0:1], v9, v19 src0_sel:WORD_0 src1_sel:DWORD
	v_cmp_eq_u32_sdwa s[24:25], v9, v36 src0_sel:WORD_0 src1_sel:DWORD
	v_lshl_add_u32 v20, v2, 1, v54
	s_and_saveexec_b64 s[26:27], s[0:1]
	global_store_short v20, v16, s[38:39]
	s_mov_b64 exec, s[26:27]
	v_addc_co_u32_e64 v2, vcc, 0, v2, s[0:1]
	v_addc_co_u32_e64 v18, vcc, 0, v18, s[24:25]
	v_add_u32_e32 v16, 0x303, v14
	v_med3_i32 v19, v18, v52, v36
	v_cmp_gt_i32_sdwa s[0:1], v9, v19 src0_sel:WORD_1 src1_sel:DWORD
	v_cmp_eq_u32_sdwa s[24:25], v9, v36 src0_sel:WORD_1 src1_sel:DWORD
	v_lshl_add_u32 v8, v2, 1, v54
	s_and_saveexec_b64 s[26:27], s[0:1]
	global_store_short v8, v16, s[38:39]
	s_mov_b64 exec, s[26:27]
	v_addc_co_u32_e64 v2, vcc, 0, v2, s[0:1]
	v_addc_co_u32_e64 v18, vcc, 0, v18, s[24:25]
	v_add_u32_e32 v8, 0x304, v14
	v_med3_i32 v19, v18, v52, v36
	v_cmp_gt_i32_sdwa s[0:1], v10, v19 src0_sel:WORD_0 src1_sel:DWORD
	v_cmp_eq_u32_sdwa s[24:25], v10, v36 src0_sel:WORD_0 src1_sel:DWORD
	v_lshl_add_u32 v16, v2, 1, v54
	s_and_saveexec_b64 s[26:27], s[0:1]
	global_store_short v16, v8, s[38:39]
	s_mov_b64 exec, s[26:27]
	v_addc_co_u32_e64 v2, vcc, 0, v2, s[0:1]
	v_addc_co_u32_e64 v18, vcc, 0, v18, s[24:25]
	v_add_u32_e32 v8, 0x305, v14
	v_med3_i32 v19, v18, v52, v36
	v_cmp_gt_i32_sdwa s[0:1], v10, v19 src0_sel:WORD_1 src1_sel:DWORD
	v_cmp_eq_u32_sdwa s[24:25], v10, v36 src0_sel:WORD_1 src1_sel:DWORD
	v_lshl_add_u32 v16, v2, 1, v54
	s_and_saveexec_b64 s[26:27], s[0:1]
	global_store_short v16, v8, s[38:39]
	s_mov_b64 exec, s[26:27]
	v_addc_co_u32_e64 v2, vcc, 0, v2, s[0:1]
	v_addc_co_u32_e64 v18, vcc, 0, v18, s[24:25]
	v_add_u32_e32 v8, 0x306, v14
	v_med3_i32 v19, v18, v52, v36
	v_cmp_gt_i32_sdwa s[0:1], v11, v19 src0_sel:WORD_0 src1_sel:DWORD
	v_cmp_eq_u32_sdwa s[24:25], v11, v36 src0_sel:WORD_0 src1_sel:DWORD
	v_lshl_add_u32 v16, v2, 1, v54
	s_and_saveexec_b64 s[26:27], s[0:1]
	global_store_short v16, v8, s[38:39]
	s_mov_b64 exec, s[26:27]
	v_addc_co_u32_e64 v2, vcc, 0, v2, s[0:1]
	v_addc_co_u32_e64 v18, vcc, 0, v18, s[24:25]
	v_add_u32_e32 v8, 0x307, v14
	v_med3_i32 v19, v18, v52, v36
	v_cmp_gt_i32_sdwa s[0:1], v11, v19 src0_sel:WORD_1 src1_sel:DWORD
	v_cmp_eq_u32_sdwa s[24:25], v11, v36 src0_sel:WORD_1 src1_sel:DWORD
	v_lshl_add_u32 v10, v2, 1, v54
	s_and_saveexec_b64 s[26:27], s[0:1]
	global_store_short v10, v8, s[38:39]
	s_mov_b64 exec, s[26:27]
	v_addc_co_u32_e64 v2, vcc, 0, v2, s[0:1]
	v_addc_co_u32_e64 v18, vcc, 0, v18, s[24:25]
	v_add_u32_e32 v8, 0x308, v14
	v_med3_i32 v19, v18, v52, v36
	v_cmp_gt_i32_sdwa s[0:1], v4, v19 src0_sel:WORD_0 src1_sel:DWORD
	v_cmp_eq_u32_sdwa s[24:25], v4, v36 src0_sel:WORD_0 src1_sel:DWORD
	v_lshl_add_u32 v10, v2, 1, v54
	s_and_saveexec_b64 s[26:27], s[0:1]
	global_store_short v10, v8, s[38:39]
	s_mov_b64 exec, s[26:27]
	v_addc_co_u32_e64 v2, vcc, 0, v2, s[0:1]
	v_addc_co_u32_e64 v18, vcc, 0, v18, s[24:25]
	v_add_u32_e32 v8, 0x309, v14
	v_med3_i32 v19, v18, v52, v36
	v_cmp_gt_i32_sdwa s[0:1], v4, v19 src0_sel:WORD_1 src1_sel:DWORD
	v_cmp_eq_u32_sdwa s[24:25], v4, v36 src0_sel:WORD_1 src1_sel:DWORD
	v_lshl_add_u32 v10, v2, 1, v54
	s_and_saveexec_b64 s[26:27], s[0:1]
	global_store_short v10, v8, s[38:39]
	s_mov_b64 exec, s[26:27]
	v_addc_co_u32_e64 v2, vcc, 0, v2, s[0:1]
	v_addc_co_u32_e64 v18, vcc, 0, v18, s[24:25]
	v_add_u32_e32 v8, 0x30a, v14
	v_med3_i32 v19, v18, v52, v36
	v_cmp_gt_i32_sdwa s[0:1], v5, v19 src0_sel:WORD_0 src1_sel:DWORD
	v_cmp_eq_u32_sdwa s[24:25], v5, v36 src0_sel:WORD_0 src1_sel:DWORD
	v_lshl_add_u32 v10, v2, 1, v54
	s_and_saveexec_b64 s[26:27], s[0:1]
	global_store_short v10, v8, s[38:39]
	s_mov_b64 exec, s[26:27]
	v_addc_co_u32_e64 v2, vcc, 0, v2, s[0:1]
	v_addc_co_u32_e64 v18, vcc, 0, v18, s[24:25]
	v_add_u32_e32 v8, 0x30b, v14
	v_med3_i32 v19, v18, v52, v36
	v_cmp_gt_i32_sdwa s[0:1], v5, v19 src0_sel:WORD_1 src1_sel:DWORD
	v_cmp_eq_u32_sdwa s[24:25], v5, v36 src0_sel:WORD_1 src1_sel:DWORD
	v_lshl_add_u32 v4, v2, 1, v54
	s_and_saveexec_b64 s[26:27], s[0:1]
	global_store_short v4, v8, s[38:39]
	s_mov_b64 exec, s[26:27]
	v_addc_co_u32_e64 v2, vcc, 0, v2, s[0:1]
	v_addc_co_u32_e64 v18, vcc, 0, v18, s[24:25]
	v_add_u32_e32 v4, 0x30c, v14
	v_med3_i32 v19, v18, v52, v36
	v_cmp_gt_i32_sdwa s[0:1], v6, v19 src0_sel:WORD_0 src1_sel:DWORD
	v_cmp_eq_u32_sdwa s[24:25], v6, v36 src0_sel:WORD_0 src1_sel:DWORD
	v_lshl_add_u32 v8, v2, 1, v54
	s_and_saveexec_b64 s[26:27], s[0:1]
	global_store_short v8, v4, s[38:39]
	s_mov_b64 exec, s[26:27]
	v_addc_co_u32_e64 v2, vcc, 0, v2, s[0:1]
	v_addc_co_u32_e64 v18, vcc, 0, v18, s[24:25]
	v_add_u32_e32 v4, 0x30d, v14
	v_med3_i32 v19, v18, v52, v36
	v_cmp_gt_i32_sdwa s[0:1], v6, v19 src0_sel:WORD_1 src1_sel:DWORD
	v_cmp_eq_u32_sdwa s[24:25], v6, v36 src0_sel:WORD_1 src1_sel:DWORD
	v_lshl_add_u32 v8, v2, 1, v54
	s_and_saveexec_b64 s[26:27], s[0:1]
	global_store_short v8, v4, s[38:39]
	s_mov_b64 exec, s[26:27]
	v_addc_co_u32_e64 v2, vcc, 0, v2, s[0:1]
	v_addc_co_u32_e64 v18, vcc, 0, v18, s[24:25]
	v_add_u32_e32 v4, 0x30e, v14
	v_med3_i32 v19, v18, v52, v36
	v_cmp_gt_i32_sdwa s[0:1], v7, v19 src0_sel:WORD_0 src1_sel:DWORD
	v_cmp_eq_u32_sdwa s[24:25], v7, v36 src0_sel:WORD_0 src1_sel:DWORD
	v_lshl_add_u32 v8, v2, 1, v54
	s_and_saveexec_b64 s[26:27], s[0:1]
	global_store_short v8, v4, s[38:39]
	s_mov_b64 exec, s[26:27]
	v_addc_co_u32_e64 v2, vcc, 0, v2, s[0:1]
	v_addc_co_u32_e64 v18, vcc, 0, v18, s[24:25]
	v_med3_i32 v19, v18, v52, v36
	v_cmp_gt_i32_sdwa s[0:1], v7, v19 src0_sel:WORD_1 src1_sel:DWORD
	v_lshl_add_u32 v8, v2, 1, v54
	v_or_b32_e32 v19, 15, v12
	s_and_saveexec_b64 s[26:27], s[0:1]
	global_store_short v8, v19, s[38:39]
	s_branch .LBB0_710
